# baseline (speedup 1.0000x reference)
.LBB1_2:
	v_and_b32_e32 v93, 15, v0
	v_lshlrev_b32_e32 v100, 4, v3
	v_lshlrev_b32_e32 v3, 6, v0
	s_movk_i32 s26, 0x3c0
	v_lshrrev_b32_e32 v92, 4, v0
	s_lshl_b32 s2, s23, 8
	s_lshl_b32 s25, s16, 6
	v_lshl_or_b32 v90, v93, 6, v100
	v_and_or_b32 v3, v3, s26, v100
	v_lshlrev_b32_e32 v0, 2, v0
	s_lshl_b32 s16, s16, 13
	s_lshl_b32 s26, s15, 7
	v_and_b32_e32 v0, 32, v0
	s_barrier
	s_add_i32 s16, s16, 0
	s_add_i32 s26, s26, 0
	v_xad_u32 v91, v90, v0, s16
	v_xad_u32 v101, v3, v0, s26
	s_mov_b32 s27, 0x18000
	s_mov_b32 s26, 16
	s_mov_b32 s28, 0
	s_mov_b32 s16, 0
	v_mov_b32_e32 v3, v2
	v_mov_b32_e32 v4, v2
	v_mov_b32_e32 v5, v2
	v_mov_b32_e32 v22, v2
	v_mov_b32_e32 v23, v2
	v_mov_b32_e32 v24, v2
	v_mov_b32_e32 v25, v2
	v_mov_b32_e32 v30, v2
	v_mov_b32_e32 v31, v2
	v_mov_b32_e32 v32, v2
	v_mov_b32_e32 v33, v2
	v_mov_b32_e32 v38, v2
	v_mov_b32_e32 v39, v2
	v_mov_b32_e32 v40, v2
	v_mov_b32_e32 v41, v2
	v_mov_b32_e32 v42, v2
	v_mov_b32_e32 v43, v2
	v_mov_b32_e32 v44, v2
	v_mov_b32_e32 v45, v2
	v_mov_b32_e32 v50, v2
	v_mov_b32_e32 v51, v2
	v_mov_b32_e32 v52, v2
	v_mov_b32_e32 v53, v2
	v_mov_b32_e32 v62, v2
	v_mov_b32_e32 v63, v2
	v_mov_b32_e32 v64, v2
	v_mov_b32_e32 v65, v2
	v_mov_b32_e32 v70, v2
	v_mov_b32_e32 v71, v2
	v_mov_b32_e32 v72, v2
	v_mov_b32_e32 v73, v2
	v_mov_b32_e32 v26, v2
	v_mov_b32_e32 v27, v2
	v_mov_b32_e32 v28, v2
	v_mov_b32_e32 v29, v2
	v_mov_b32_e32 v34, v2
	v_mov_b32_e32 v35, v2
	v_mov_b32_e32 v36, v2
	v_mov_b32_e32 v37, v2
	v_mov_b32_e32 v46, v2
	v_mov_b32_e32 v47, v2
	v_mov_b32_e32 v48, v2
	v_mov_b32_e32 v49, v2
	v_mov_b32_e32 v54, v2
	v_mov_b32_e32 v55, v2
	v_mov_b32_e32 v56, v2
	v_mov_b32_e32 v57, v2
	v_mov_b32_e32 v58, v2
	v_mov_b32_e32 v59, v2
	v_mov_b32_e32 v60, v2
	v_mov_b32_e32 v61, v2
	v_mov_b32_e32 v66, v2
	v_mov_b32_e32 v67, v2
	v_mov_b32_e32 v68, v2
	v_mov_b32_e32 v69, v2
	v_mov_b32_e32 v74, v2
	v_mov_b32_e32 v75, v2
	v_mov_b32_e32 v76, v2
	v_mov_b32_e32 v77, v2
	v_mov_b32_e32 v78, v2
	v_mov_b32_e32 v79, v2
	v_mov_b32_e32 v80, v2
	v_mov_b32_e32 v81, v2
	s_mov_b32 s29, s16
	s_lshl_b32 s16, s28, 2
	s_or_b32 s16, s16, s23
	s_lshl_b64 s[30:31], s[16:17], 19
	s_add_u32 s16, s6, s30
	s_addc_u32 s31, s7, s31
	s_lshl_b32 s33, s3, 7
	s_ashr_i32 s35, s33, 31
	s_add_u32 s30, s16, s33
	s_addc_u32 s31, s31, s35
	s_add_u32 s34, s4, s33
	s_addc_u32 s35, s5, s35
	s_add_i32 s16, s19, s27
.LBB1_3:
	v_add_u32_e32 v0, s29, v101
	ds_read_b128 v[94:97], v0 offset:16384
	ds_read_b128 v[102:105], v0 offset:17408
	ds_read_b128 v[106:109], v0 offset:18432
	ds_read_b128 v[110:113], v0 offset:19456
	ds_read_b128 v[114:117], v0 offset:32768
	ds_read_b128 v[118:121], v0 offset:33792
	ds_read_b128 v[122:125], v0 offset:34816
	s_add_i32 m0, s16, 0x4000
	ds_read_b128 v[126:129], v0 offset:35840
	global_load_lds_dwordx4 v84, s[30:31]
	v_add_u32_e32 v0, s29, v91
	ds_read_b128 v[130:133], v0
	ds_read_b128 v[134:137], v0 offset:1024
	s_add_i32 m0, s16, 0x6000
	ds_read_b128 v[138:141], v0 offset:2048
	global_load_lds_dwordx4 v88, s[30:31]
	ds_read_b128 v[142:145], v0 offset:3072
	ds_read_b128 v[146:149], v0 offset:4096
	s_mov_b32 m0, s16
	ds_read_b128 v[150:153], v0 offset:5120
	global_load_lds_dwordx4 v82, s[34:35]
	ds_read_b128 v[154:157], v0 offset:6144
	ds_read_b128 v[158:161], v0 offset:7168
	s_waitcnt vmcnt(3)
	s_waitcnt lgkmcnt(0)
	s_barrier
	s_setprio 1
	s_waitcnt lgkmcnt(0)
	v_mfma_f32_16x16x32_f16 v[78:81], v[94:97], v[130:133], v[78:81]
	s_add_u32 s30, s30, 0x40000
	s_addc_u32 s31, s31, 0
	s_add_i32 m0, s16, 0x8000
	v_mfma_f32_16x16x32_f16 v[74:77], v[106:109], v[130:133], v[74:77]
	global_load_lds_dwordx4 v84, s[30:31]
	s_add_i32 m0, s16, 0xa000
	v_mfma_f32_16x16x32_f16 v[66:69], v[94:97], v[138:141], v[66:69]
	global_load_lds_dwordx4 v88, s[30:31]
	s_add_i32 m0, s16, 0x2000
	v_mfma_f32_16x16x32_f16 v[58:61], v[106:109], v[138:141], v[58:61]
	global_load_lds_dwordx4 v86, s[34:35]
	v_mfma_f32_16x16x32_f16 v[78:81], v[102:105], v[134:137], v[78:81]
	s_add_i32 s3, s3, 1
	v_mfma_f32_16x16x32_f16 v[74:77], v[110:113], v[134:137], v[74:77]
	s_bitcmp1_b32 s3, 4
	v_mfma_f32_16x16x32_f16 v[66:69], v[102:105], v[142:145], v[66:69]
	s_addc_u32 s28, s28, 0
	v_mfma_f32_16x16x32_f16 v[58:61], v[110:113], v[142:145], v[58:61]
	s_and_b32 s3, s3, 15
	v_mfma_f32_16x16x32_f16 v[54:57], v[94:97], v[146:149], v[54:57]
	s_add_i32 s26, s26, -1
	v_mfma_f32_16x16x32_f16 v[46:49], v[106:109], v[146:149], v[46:49]
	s_mov_b32 s38, s29
	v_mfma_f32_16x16x32_f16 v[34:37], v[94:97], v[154:157], v[34:37]
	s_mov_b32 s29, s24
	v_mfma_f32_16x16x32_f16 v[26:29], v[106:109], v[154:157], v[26:29]
	s_mov_b32 s24, s27
	v_mfma_f32_16x16x32_f16 v[54:57], v[102:105], v[150:153], v[54:57]
	s_mov_b32 s27, s38
	v_mfma_f32_16x16x32_f16 v[46:49], v[110:113], v[150:153], v[46:49]
	s_lshl_b32 s16, s28, 2
	v_mfma_f32_16x16x32_f16 v[34:37], v[102:105], v[158:161], v[34:37]
	s_or_b32 s16, s16, s23
	v_mfma_f32_16x16x32_f16 v[26:29], v[110:113], v[158:161], v[26:29]
	s_lshl_b64 s[30:31], s[16:17], 19
	v_mfma_f32_16x16x32_f16 v[70:73], v[114:117], v[130:133], v[70:73]
	s_add_u32 s16, s6, s30
	v_mfma_f32_16x16x32_f16 v[62:65], v[122:125], v[130:133], v[62:65]
	s_addc_u32 s31, s7, s31
	v_mfma_f32_16x16x32_f16 v[50:53], v[114:117], v[138:141], v[50:53]
	s_lshl_b32 s33, s3, 7
	v_mfma_f32_16x16x32_f16 v[42:45], v[122:125], v[138:141], v[42:45]
	s_ashr_i32 s35, s33, 31
	v_mfma_f32_16x16x32_f16 v[70:73], v[118:121], v[134:137], v[70:73]
	s_add_u32 s30, s16, s33
	v_mfma_f32_16x16x32_f16 v[62:65], v[126:129], v[134:137], v[62:65]
	s_addc_u32 s31, s31, s35
	v_mfma_f32_16x16x32_f16 v[50:53], v[118:121], v[142:145], v[50:53]
	s_add_u32 s34, s4, s33
	v_mfma_f32_16x16x32_f16 v[42:45], v[126:129], v[142:145], v[42:45]
	s_addc_u32 s35, s5, s35
	v_mfma_f32_16x16x32_f16 v[38:41], v[114:117], v[146:149], v[38:41]
	s_add_i32 s16, s19, s27
	v_mfma_f32_16x16x32_f16 v[30:33], v[122:125], v[146:149], v[30:33]
	s_cmp_lg_u32 s26, 0
	v_mfma_f32_16x16x32_f16 v[22:25], v[114:117], v[154:157], v[22:25]
	v_mfma_f32_16x16x32_f16 v[2:5], v[122:125], v[154:157], v[2:5]
	v_mfma_f32_16x16x32_f16 v[38:41], v[118:121], v[150:153], v[38:41]
	v_mfma_f32_16x16x32_f16 v[30:33], v[126:129], v[150:153], v[30:33]
	v_mfma_f32_16x16x32_f16 v[22:25], v[118:121], v[158:161], v[22:25]
	v_mfma_f32_16x16x32_f16 v[2:5], v[126:129], v[158:161], v[2:5]
	s_setprio 0
	s_barrier
	s_cbranch_scc1 .LBB1_3
	s_mov_b32 s16, s29
	s_mov_b32 s29, s27
	s_lshl_b32 s3, s14, 7
	s_add_i32 s17, s25, s3
	s_ashr_i32 s3, s17, 1
	s_lshr_b32 s14, s17, 5
	s_or_b32 s24, s15, s2
	s_and_b32 s14, s14, 62
	s_and_b32 s27, s3, 0xfffffc00
	v_or_b32_e32 v105, s24, v1
	v_lshlrev_b32_e32 v98, 4, v93
	v_or_b32_e32 v102, 16, v93
	v_or_b32_e32 v103, 32, v93
	v_or_b32_e32 v104, 48, v93
	v_mov_b32_e32 v93, 0
	s_and_b32 s16, s24, 0x340
	v_lshlrev_b32_e32 v95, 6, v105
	s_or_b32 s2, s27, s14
	v_lshlrev_b32_e32 v0, 9, v92
	v_and_b32_e32 v110, 0xc00, v95
	v_mov_b32_e32 v111, v93
	s_or_b32 s14, s2, s16
	v_and_b32_e32 v92, 0x200, v0
	v_lshl_add_u64 v[110:111], s[8:9], 0, v[110:111]
	s_or_b32 s30, s14, 0x80
	s_mov_b32 s3, 0
	v_mov_b32_e32 v99, v93
	v_lshl_add_u64 v[110:111], v[110:111], 0, v[92:93]
	s_mov_b32 s2, 0x3e38aa3b
	v_pk_add_f32 v[72:73], v[12:13], v[72:73]
	v_pk_add_f32 v[70:71], v[10:11], v[70:71]
	v_pk_add_f32 v[64:65], v[8:9], v[64:65]
	v_pk_add_f32 v[62:63], v[6:7], v[62:63]
	s_ashr_i32 s31, s30, 31
	v_lshl_add_u64 v[112:113], v[110:111], 0, v[98:99]
	v_pk_mul_f32 v[72:73], v[72:73], s[2:3] op_sel_hi:[1,0]
	v_pk_mul_f32 v[70:71], v[70:71], s[2:3] op_sel_hi:[1,0]
	v_pk_mul_f32 v[64:65], v[64:65], s[2:3] op_sel_hi:[1,0]
	v_pk_mul_f32 v[62:63], v[62:63], s[2:3] op_sel_hi:[1,0]
	s_lshl_b64 s[30:31], s[30:31], 12
	v_lshlrev_b32_e32 v96, 4, v102
	v_mov_b32_e32 v97, v93
	v_pk_add_f32 v[80:81], v[20:21], v[80:81]
	v_pk_add_f32 v[78:79], v[18:19], v[78:79]
	v_pk_add_f32 v[74:75], v[14:15], v[74:75]
	s_ashr_i32 s15, s14, 31
	v_cvt_pk_f16_f32 v70, v70, v71
	v_cvt_pk_f16_f32 v71, v72, v73
	v_cvt_pk_f16_f32 v72, v62, v63
	v_cvt_pk_f16_f32 v73, v64, v65
	v_lshl_add_u64 v[62:63], v[112:113], 0, s[30:31]
	v_pk_add_f32 v[58:59], v[14:15], v[58:59]
	v_pk_mul_f32 v[80:81], v[80:81], s[2:3] op_sel_hi:[1,0]
	v_pk_mul_f32 v[78:79], v[78:79], s[2:3] op_sel_hi:[1,0]
	v_pk_mul_f32 v[74:75], v[74:75], s[2:3] op_sel_hi:[1,0]
	s_lshl_b64 s[28:29], s[14:15], 12
	global_store_dwordx4 v[62:63], v[70:73], off
	v_pk_add_f32 v[62:63], v[20:21], v[68:69]
	v_pk_add_f32 v[64:65], v[18:19], v[66:67]
	v_lshl_add_u64 v[70:71], v[110:111], 0, v[96:97]
	v_pk_mul_f32 v[58:59], v[58:59], s[2:3] op_sel_hi:[1,0]
	v_pk_add_f32 v[52:53], v[12:13], v[52:53]
	v_pk_add_f32 v[50:51], v[10:11], v[50:51]
	v_pk_add_f32 v[44:45], v[8:9], v[44:45]
	v_pk_add_f32 v[42:43], v[6:7], v[42:43]
	v_lshlrev_b32_e32 v0, 4, v103
	v_cvt_pk_f16_f32 v78, v78, v79
	v_cvt_pk_f16_f32 v79, v80, v81
	v_cvt_pk_f16_f32 v80, v74, v75
	v_lshl_add_u64 v[74:75], v[112:113], 0, s[28:29]
	v_pk_mul_f32 v[66:67], v[62:63], s[2:3] op_sel_hi:[1,0]
	v_pk_mul_f32 v[62:63], v[64:65], s[2:3] op_sel_hi:[1,0]
	v_cvt_pk_f16_f32 v64, v58, v59
	v_lshl_add_u64 v[58:59], v[70:71], 0, s[28:29]
	v_pk_mul_f32 v[52:53], v[52:53], s[2:3] op_sel_hi:[1,0]
	v_pk_mul_f32 v[50:51], v[50:51], s[2:3] op_sel_hi:[1,0]
	v_pk_mul_f32 v[44:45], v[44:45], s[2:3] op_sel_hi:[1,0]
	v_pk_mul_f32 v[42:43], v[42:43], s[2:3] op_sel_hi:[1,0]
	s_or_b32 s28, s14, 1
	s_or_b32 s14, s14, 0x81
	v_and_b32_e32 v106, 0xf0, v0
	v_mov_b32_e32 v107, v93
	v_cvt_pk_f16_f32 v50, v50, v51
	v_cvt_pk_f16_f32 v51, v52, v53
	v_cvt_pk_f16_f32 v52, v42, v43
	v_cvt_pk_f16_f32 v53, v44, v45
	v_lshl_add_u64 v[42:43], v[70:71], 0, s[30:31]
	v_pk_add_f32 v[40:41], v[12:13], v[40:41]
	v_pk_add_f32 v[38:39], v[10:11], v[38:39]
	v_pk_add_f32 v[32:33], v[8:9], v[32:33]
	v_pk_add_f32 v[30:31], v[6:7], v[30:31]
	s_ashr_i32 s15, s14, 31
	v_lshlrev_b32_e32 v94, 4, v104
	global_store_dwordx4 v[42:43], v[50:53], off
	v_pk_mul_f32 v[40:41], v[40:41], s[2:3] op_sel_hi:[1,0]
	v_pk_mul_f32 v[38:39], v[38:39], s[2:3] op_sel_hi:[1,0]
	v_lshl_add_u64 v[50:51], v[110:111], 0, v[106:107]
	v_pk_mul_f32 v[32:33], v[32:33], s[2:3] op_sel_hi:[1,0]
	v_pk_mul_f32 v[30:31], v[30:31], s[2:3] op_sel_hi:[1,0]
	s_lshl_b64 s[14:15], s[14:15], 12
	v_and_b32_e32 v108, 0x1f0, v94
	v_mov_b32_e32 v109, v93
	v_pk_add_f32 v[42:43], v[20:21], v[56:57]
	v_pk_add_f32 v[44:45], v[18:19], v[54:55]
	v_pk_add_f32 v[46:47], v[14:15], v[46:47]
	s_ashr_i32 s29, s28, 31
	v_cvt_pk_f16_f32 v38, v38, v39
	v_cvt_pk_f16_f32 v39, v40, v41
	v_cvt_pk_f16_f32 v40, v30, v31
	v_cvt_pk_f16_f32 v41, v32, v33
	v_lshl_add_u64 v[30:31], v[50:51], 0, s[14:15]
	v_pk_add_f32 v[20:21], v[20:21], v[36:37]
	v_pk_add_f32 v[18:19], v[18:19], v[34:35]
	v_pk_add_f32 v[14:15], v[14:15], v[26:27]
	v_pk_add_f32 v[76:77], v[16:17], v[76:77]
	v_pk_add_f32 v[60:61], v[16:17], v[60:61]
	v_pk_mul_f32 v[52:53], v[42:43], s[2:3] op_sel_hi:[1,0]
	v_pk_mul_f32 v[42:43], v[44:45], s[2:3] op_sel_hi:[1,0]
	v_pk_add_f32 v[44:45], v[16:17], v[48:49]
	s_lshl_b64 s[28:29], s[28:29], 12
	global_store_dwordx4 v[30:31], v[38:41], off
	v_lshl_add_u64 v[30:31], v[110:111], 0, v[108:109]
	v_pk_mul_f32 v[20:21], v[20:21], s[2:3] op_sel_hi:[1,0]
	v_pk_mul_f32 v[18:19], v[18:19], s[2:3] op_sel_hi:[1,0]
	v_pk_add_f32 v[16:17], v[16:17], v[28:29]
	v_pk_mul_f32 v[14:15], v[14:15], s[2:3] op_sel_hi:[1,0]
	v_pk_add_f32 v[12:13], v[12:13], v[24:25]
	v_pk_add_f32 v[10:11], v[10:11], v[22:23]
	v_pk_add_f32 v[4:5], v[8:9], v[4:5]
	v_pk_add_f32 v[2:3], v[6:7], v[2:3]
	v_pk_mul_f32 v[76:77], v[76:77], s[2:3] op_sel_hi:[1,0]
	v_pk_mul_f32 v[60:61], v[60:61], s[2:3] op_sel_hi:[1,0]
	v_pk_mul_f32 v[48:49], v[44:45], s[2:3] op_sel_hi:[1,0]
	v_pk_mul_f32 v[44:45], v[46:47], s[2:3] op_sel_hi:[1,0]
	v_lshl_add_u64 v[46:47], v[50:51], 0, s[28:29]
	v_cvt_pk_f16_f32 v18, v18, v19
	v_cvt_pk_f16_f32 v19, v20, v21
	v_pk_mul_f32 v[16:17], v[16:17], s[2:3] op_sel_hi:[1,0]
	v_cvt_pk_f16_f32 v20, v14, v15
	v_lshl_add_u64 v[14:15], v[30:31], 0, s[28:29]
	v_pk_mul_f32 v[12:13], v[12:13], s[2:3] op_sel_hi:[1,0]
	v_pk_mul_f32 v[10:11], v[10:11], s[2:3] op_sel_hi:[1,0]
	v_pk_mul_f32 v[4:5], v[4:5], s[2:3] op_sel_hi:[1,0]
	v_pk_mul_f32 v[2:3], v[2:3], s[2:3] op_sel_hi:[1,0]
	s_add_u32 s28, s20, s22
	v_cvt_pk_f16_f32 v81, v76, v77
	v_cvt_pk_f16_f32 v62, v62, v63
	v_cvt_pk_f16_f32 v63, v66, v67
	v_cvt_pk_f16_f32 v65, v60, v61
	v_cvt_pk_f16_f32 v42, v42, v43
	v_cvt_pk_f16_f32 v43, v52, v53
	v_cvt_pk_f16_f32 v44, v44, v45
	v_cvt_pk_f16_f32 v45, v48, v49
	v_cvt_pk_f16_f32 v21, v16, v17
	v_cvt_pk_f16_f32 v10, v10, v11
	v_cvt_pk_f16_f32 v11, v12, v13
	v_cvt_pk_f16_f32 v12, v2, v3
	v_cvt_pk_f16_f32 v13, v4, v5
	v_lshl_add_u64 v[2:3], v[30:31], 0, s[14:15]
	s_addc_u32 s29, s21, 0
	v_lshlrev_b32_e32 v92, 2, v1
	global_store_dwordx4 v[74:75], v[78:81], off
	global_store_dwordx4 v[58:59], v[62:65], off
	global_store_dwordx4 v[46:47], v[42:45], off
	global_store_dwordx4 v[14:15], v[18:21], off
	global_store_dwordx4 v[2:3], v[10:13], off
	v_lshl_add_u64 v[2:3], s[28:29], 0, v[92:93]
	s_mov_b64 s[28:29], 0x1000
	v_lshl_add_u64 v[10:11], v[2:3], 0, s[28:29]
	global_load_dwordx4 v[22:25], v[10:11], off
	global_load_dwordx4 v[14:17], v[10:11], off offset:16
	global_load_dwordx4 v[6:9], v[10:11], off offset:512
	global_load_dwordx4 v[2:5], v[10:11], off offset:528
	s_mov_b32 s25, 1
	s_mov_b32 s26, 16
	s_mov_b32 s14, 2
	s_mov_b32 s15, 0x18000
	s_mov_b32 s2, 0xc000
	s_mov_b32 s27, 0
	v_mov_b32_e32 v10, v93
	v_mov_b32_e32 v11, v93
	v_mov_b32_e32 v12, v93
	v_mov_b32_e32 v13, v93
	v_mov_b32_e32 v18, v93
	v_mov_b32_e32 v19, v93
	v_mov_b32_e32 v20, v93
	v_mov_b32_e32 v21, v93
	v_mov_b32_e32 v26, v93
	v_mov_b32_e32 v27, v93
	v_mov_b32_e32 v28, v93
	v_mov_b32_e32 v29, v93
	v_mov_b32_e32 v34, v93
	v_mov_b32_e32 v35, v93
	v_mov_b32_e32 v36, v93
	v_mov_b32_e32 v37, v93
	v_mov_b32_e32 v42, v93
	v_mov_b32_e32 v43, v93
	v_mov_b32_e32 v44, v93
	v_mov_b32_e32 v45, v93
	v_mov_b32_e32 v50, v93
	v_mov_b32_e32 v51, v93
	v_mov_b32_e32 v52, v93
	v_mov_b32_e32 v53, v93
	v_mov_b32_e32 v62, v93
	v_mov_b32_e32 v63, v93
	v_mov_b32_e32 v64, v93
	v_mov_b32_e32 v65, v93
	v_mov_b32_e32 v70, v93
	v_mov_b32_e32 v71, v93
	v_mov_b32_e32 v72, v93
	v_mov_b32_e32 v73, v93
	v_mov_b32_e32 v30, v93
	v_mov_b32_e32 v31, v93
	v_mov_b32_e32 v32, v93
	v_mov_b32_e32 v33, v93
	v_mov_b32_e32 v38, v93
	v_mov_b32_e32 v39, v93
	v_mov_b32_e32 v40, v93
	v_mov_b32_e32 v41, v93
	v_mov_b32_e32 v46, v93
	v_mov_b32_e32 v47, v93
	v_mov_b32_e32 v48, v93
	v_mov_b32_e32 v49, v93
	v_mov_b32_e32 v54, v93
	v_mov_b32_e32 v55, v93
	v_mov_b32_e32 v56, v93
	v_mov_b32_e32 v57, v93
	v_mov_b32_e32 v58, v93
	v_mov_b32_e32 v59, v93
	v_mov_b32_e32 v60, v93
	v_mov_b32_e32 v61, v93
	v_mov_b32_e32 v66, v93
	v_mov_b32_e32 v67, v93
	v_mov_b32_e32 v68, v93
	v_mov_b32_e32 v69, v93
	v_mov_b32_e32 v74, v93
	v_mov_b32_e32 v75, v93
	v_mov_b32_e32 v76, v93
	v_mov_b32_e32 v77, v93
	v_mov_b32_e32 v78, v93
	v_mov_b32_e32 v79, v93
	v_mov_b32_e32 v80, v93
	v_mov_b32_e32 v81, v93
	s_mov_b32 s28, s2
	s_lshl_b32 s2, s25, 2
	s_or_b32 s2, s2, s23
	s_lshl_b64 s[30:31], s[2:3], 19
	s_add_u32 s2, s6, s30
	s_addc_u32 s29, s7, s31
	s_lshl_b32 s33, s14, 7
	s_ashr_i32 s35, s33, 31
	s_add_u32 s30, s2, s33
	s_addc_u32 s31, s29, s35
	s_add_u32 s34, s4, s33
	s_addc_u32 s35, s5, s35
	s_add_i32 s2, s19, s27
.LBB1_5:
	v_add_u32_e32 v1, s28, v101
	ds_read_b128 v[106:109], v1 offset:16384
	ds_read_b128 v[110:113], v1 offset:17408
	ds_read_b128 v[114:117], v1 offset:18432
	ds_read_b128 v[118:121], v1 offset:19456
	ds_read_b128 v[122:125], v1 offset:32768
	ds_read_b128 v[126:129], v1 offset:33792
	ds_read_b128 v[130:133], v1 offset:34816
	s_add_i32 m0, s2, 0x4000
	ds_read_b128 v[134:137], v1 offset:35840
	global_load_lds_dwordx4 v84, s[30:31]
	v_add_u32_e32 v1, s28, v91
	ds_read_b128 v[138:141], v1
	ds_read_b128 v[142:145], v1 offset:1024
	s_add_i32 m0, s2, 0x6000
	ds_read_b128 v[146:149], v1 offset:2048
	global_load_lds_dwordx4 v88, s[30:31]
	ds_read_b128 v[150:153], v1 offset:3072
	ds_read_b128 v[154:157], v1 offset:4096
	s_mov_b32 m0, s2
	ds_read_b128 v[158:161], v1 offset:5120
	global_load_lds_dwordx4 v82, s[34:35]
	ds_read_b128 v[162:165], v1 offset:6144
	ds_read_b128 v[166:169], v1 offset:7168
	s_waitcnt vmcnt(3)
	s_waitcnt lgkmcnt(0)
	s_barrier
	s_setprio 1
	s_waitcnt lgkmcnt(0)
	v_mfma_f32_16x16x32_f16 v[78:81], v[106:109], v[138:141], v[78:81]
	s_add_u32 s30, s30, 0x40000
	s_addc_u32 s31, s31, 0
	s_add_i32 m0, s2, 0x8000
	v_mfma_f32_16x16x32_f16 v[74:77], v[114:117], v[138:141], v[74:77]
	global_load_lds_dwordx4 v84, s[30:31]
	s_add_i32 m0, s2, 0xa000
	v_mfma_f32_16x16x32_f16 v[66:69], v[106:109], v[146:149], v[66:69]
	global_load_lds_dwordx4 v88, s[30:31]
	s_add_i32 m0, s2, 0x2000
	v_mfma_f32_16x16x32_f16 v[58:61], v[114:117], v[146:149], v[58:61]
	global_load_lds_dwordx4 v86, s[34:35]
	v_mfma_f32_16x16x32_f16 v[78:81], v[110:113], v[142:145], v[78:81]
	s_add_i32 s14, s14, 1
	v_mfma_f32_16x16x32_f16 v[74:77], v[118:121], v[142:145], v[74:77]
	s_bitcmp1_b32 s14, 4
	v_mfma_f32_16x16x32_f16 v[66:69], v[110:113], v[150:153], v[66:69]
	s_addc_u32 s25, s25, 0
	v_mfma_f32_16x16x32_f16 v[58:61], v[118:121], v[150:153], v[58:61]
	s_and_b32 s14, s14, 15
	v_mfma_f32_16x16x32_f16 v[54:57], v[106:109], v[154:157], v[54:57]
	s_add_i32 s26, s26, -1
	v_mfma_f32_16x16x32_f16 v[46:49], v[114:117], v[154:157], v[46:49]
	s_mov_b32 s38, s28
	v_mfma_f32_16x16x32_f16 v[38:41], v[106:109], v[162:165], v[38:41]
	s_mov_b32 s28, s15
	v_mfma_f32_16x16x32_f16 v[30:33], v[114:117], v[162:165], v[30:33]
	s_mov_b32 s15, s27
	v_mfma_f32_16x16x32_f16 v[54:57], v[110:113], v[158:161], v[54:57]
	s_mov_b32 s27, s38
	v_mfma_f32_16x16x32_f16 v[46:49], v[118:121], v[158:161], v[46:49]
	s_lshl_b32 s2, s25, 2
	v_mfma_f32_16x16x32_f16 v[38:41], v[110:113], v[166:169], v[38:41]
	s_or_b32 s2, s2, s23
	v_mfma_f32_16x16x32_f16 v[30:33], v[118:121], v[166:169], v[30:33]
	s_lshl_b64 s[30:31], s[2:3], 19
	v_mfma_f32_16x16x32_f16 v[70:73], v[122:125], v[138:141], v[70:73]
	s_add_u32 s2, s6, s30
	v_mfma_f32_16x16x32_f16 v[62:65], v[130:133], v[138:141], v[62:65]
	s_addc_u32 s29, s7, s31
	v_mfma_f32_16x16x32_f16 v[50:53], v[122:125], v[146:149], v[50:53]
	s_lshl_b32 s33, s14, 7
	v_mfma_f32_16x16x32_f16 v[42:45], v[130:133], v[146:149], v[42:45]
	s_ashr_i32 s35, s33, 31
	v_mfma_f32_16x16x32_f16 v[70:73], v[126:129], v[142:145], v[70:73]
	s_add_u32 s30, s2, s33
	v_mfma_f32_16x16x32_f16 v[62:65], v[134:137], v[142:145], v[62:65]
	s_addc_u32 s31, s29, s35
	v_mfma_f32_16x16x32_f16 v[50:53], v[126:129], v[150:153], v[50:53]
	s_add_u32 s34, s4, s33
	v_mfma_f32_16x16x32_f16 v[42:45], v[134:137], v[150:153], v[42:45]
	s_addc_u32 s35, s5, s35
	v_mfma_f32_16x16x32_f16 v[34:37], v[122:125], v[154:157], v[34:37]
	s_add_i32 s2, s19, s27
	v_mfma_f32_16x16x32_f16 v[26:29], v[130:133], v[154:157], v[26:29]
	s_cmp_lg_u32 s26, 0
	v_mfma_f32_16x16x32_f16 v[18:21], v[122:125], v[162:165], v[18:21]
	v_mfma_f32_16x16x32_f16 v[10:13], v[130:133], v[162:165], v[10:13]
	v_mfma_f32_16x16x32_f16 v[34:37], v[126:129], v[158:161], v[34:37]
	v_mfma_f32_16x16x32_f16 v[26:29], v[134:137], v[158:161], v[26:29]
	v_mfma_f32_16x16x32_f16 v[18:21], v[126:129], v[166:169], v[18:21]
	v_mfma_f32_16x16x32_f16 v[10:13], v[134:137], v[166:169], v[10:13]
	s_setprio 0
	s_barrier
	s_cbranch_scc1 .LBB1_5
	s_mov_b32 s2, s28
	s_mov_b32 s28, s27
	s_ashr_i32 s2, s17, 7
	s_and_b32 s3, s2, -16
	s_or_b32 s2, s3, 2
	s_sub_u32 s14, s10, s8
	s_subb_u32 s11, s11, s9
	s_bfe_u32 s6, s17, 0x50006
	s_add_u32 s14, s8, s14
	s_addc_u32 s15, s9, s11
	s_lshr_b32 s11, s24, 6
	s_or_b32 s17, s11, s3
	s_lshl_b32 s17, s17, 8
	s_lshl_b32 s23, s6, 3
	v_bfe_u32 v93, v105, 3, 3
	v_pk_add_f32 v[80:81], v[24:25], v[80:81]
	v_pk_add_f32 v[78:79], v[22:23], v[78:79]
	v_pk_add_f32 v[74:75], v[14:15], v[74:75]
	s_or_b32 s17, s17, s23
	s_or_b32 s11, s2, s11
	v_cvt_pk_f16_f32 v78, v78, v79
	v_cvt_pk_f16_f32 v79, v80, v81
	v_cvt_pk_f16_f32 v80, v74, v75
	v_or_b32_e32 v74, s17, v93
	s_lshl_b32 s11, s11, 8
	v_ashrrev_i32_e32 v75, 31, v74
	v_pk_add_f32 v[72:73], v[8:9], v[72:73]
	v_pk_add_f32 v[70:71], v[6:7], v[70:71]
	v_pk_add_f32 v[62:63], v[2:3], v[62:63]
	s_or_b32 s11, s11, s23
	v_lshlrev_b64 v[74:75], 10, v[74:75]
	v_cvt_pk_f16_f32 v70, v70, v71
	v_cvt_pk_f16_f32 v71, v72, v73
	v_cvt_pk_f16_f32 v72, v62, v63
	v_or_b32_e32 v62, s11, v93
	v_pk_add_f32 v[76:77], v[16:17], v[76:77]
	v_lshl_add_u64 v[74:75], s[14:15], 0, v[74:75]
	v_ashrrev_i32_e32 v63, 31, v62
	v_cvt_pk_f16_f32 v81, v76, v77
	v_lshl_add_u64 v[76:77], v[74:75], 0, v[98:99]
	v_lshlrev_b64 v[62:63], 10, v[62:63]
	global_store_dwordx4 v[76:77], v[78:81], off
	v_pk_add_f32 v[64:65], v[4:5], v[64:65]
	v_lshl_add_u64 v[76:77], s[14:15], 0, v[62:63]
	v_cvt_pk_f16_f32 v73, v64, v65
	v_lshl_add_u64 v[62:63], v[76:77], 0, v[98:99]
	global_store_dwordx4 v[62:63], v[70:73], off
	v_pk_add_f32 v[64:65], v[24:25], v[68:69]
	v_pk_add_f32 v[62:63], v[22:23], v[66:67]
	v_pk_add_f32 v[60:61], v[16:17], v[60:61]
	v_pk_add_f32 v[58:59], v[14:15], v[58:59]
	v_pk_add_f32 v[52:53], v[8:9], v[52:53]
	v_pk_add_f32 v[50:51], v[6:7], v[50:51]
	v_pk_add_f32 v[44:45], v[4:5], v[44:45]
	v_pk_add_f32 v[42:43], v[2:3], v[42:43]
	v_cvt_pk_f16_f32 v62, v62, v63
	v_cvt_pk_f16_f32 v63, v64, v65
	v_cvt_pk_f16_f32 v64, v58, v59
	v_cvt_pk_f16_f32 v65, v60, v61
	v_lshl_add_u64 v[58:59], v[74:75], 0, v[96:97]
	v_cvt_pk_f16_f32 v50, v50, v51
	v_cvt_pk_f16_f32 v51, v52, v53
	v_cvt_pk_f16_f32 v52, v42, v43
	v_cvt_pk_f16_f32 v53, v44, v45
	v_lshl_add_u64 v[42:43], v[76:77], 0, v[96:97]
	v_mov_b32_e32 v1, 0
	global_store_dwordx4 v[58:59], v[62:65], off
	global_store_dwordx4 v[42:43], v[50:53], off
	v_pk_add_f32 v[44:45], v[24:25], v[56:57]
	v_pk_add_f32 v[42:43], v[22:23], v[54:55]
	v_mov_b32_e32 v95, v1
	v_cvt_pk_f16_f32 v42, v42, v43
	v_cvt_pk_f16_f32 v43, v44, v45
	v_pk_add_f32 v[48:49], v[16:17], v[48:49]
	v_pk_add_f32 v[44:45], v[14:15], v[46:47]
	v_pk_add_f32 v[36:37], v[8:9], v[36:37]
	v_pk_add_f32 v[34:35], v[6:7], v[34:35]
	v_pk_add_f32 v[28:29], v[4:5], v[28:29]
	v_pk_add_f32 v[26:27], v[2:3], v[26:27]
	v_pk_add_f32 v[24:25], v[24:25], v[40:41]
	v_pk_add_f32 v[22:23], v[22:23], v[38:39]
	v_pk_add_f32 v[16:17], v[16:17], v[32:33]
	v_pk_add_f32 v[14:15], v[14:15], v[30:31]
	v_pk_add_f32 v[8:9], v[8:9], v[20:21]
	v_pk_add_f32 v[6:7], v[6:7], v[18:19]
	v_pk_add_f32 v[4:5], v[4:5], v[12:13]
	v_pk_add_f32 v[2:3], v[2:3], v[10:11]
	s_add_u32 s14, s20, s22
	v_cvt_pk_f16_f32 v44, v44, v45
	v_cvt_pk_f16_f32 v45, v48, v49
	v_lshl_add_u64 v[46:47], v[74:75], 0, v[0:1]
	v_cvt_pk_f16_f32 v34, v34, v35
	v_cvt_pk_f16_f32 v35, v36, v37
	v_cvt_pk_f16_f32 v36, v26, v27
	v_cvt_pk_f16_f32 v37, v28, v29
	v_lshl_add_u64 v[26:27], v[76:77], 0, v[0:1]
	v_cvt_pk_f16_f32 v22, v22, v23
	v_cvt_pk_f16_f32 v23, v24, v25
	v_cvt_pk_f16_f32 v24, v14, v15
	v_cvt_pk_f16_f32 v25, v16, v17
	v_lshl_add_u64 v[14:15], v[74:75], 0, v[94:95]
	v_cvt_pk_f16_f32 v6, v6, v7
	v_cvt_pk_f16_f32 v7, v8, v9
	v_cvt_pk_f16_f32 v8, v2, v3
	v_cvt_pk_f16_f32 v9, v4, v5
	v_lshl_add_u64 v[2:3], v[76:77], 0, v[94:95]
	s_addc_u32 s15, s21, 0
	v_mov_b32_e32 v93, v1
	global_store_dwordx4 v[46:47], v[42:45], off
	global_store_dwordx4 v[26:27], v[34:37], off
	global_store_dwordx4 v[14:15], v[22:25], off
	global_store_dwordx4 v[2:3], v[6:9], off
	v_lshl_add_u64 v[2:3], s[14:15], 0, v[92:93]
	s_mov_b64 s[14:15], 0x2000
	v_lshl_add_u64 v[2:3], v[2:3], 0, s[14:15]
	global_load_dwordx4 v[20:23], v[2:3], off
	global_load_dwordx4 v[12:15], v[2:3], off offset:16
	global_load_dwordx4 v[8:11], v[2:3], off offset:512
	global_load_dwordx4 v[4:7], v[2:3], off offset:528
	s_add_u32 s11, s12, 0x400000
	s_mov_b32 s7, 2
	v_and_b32_e32 v106, 56, v105
	s_mov_b32 s10, 0
	s_addc_u32 s12, s13, 0
	s_mov_b32 s14, 0xc000
	s_mov_b32 s17, 0x18000
	s_mov_b32 s13, 16
	v_mov_b32_e32 v0, v1
	v_mov_b32_e32 v2, v1
	v_mov_b32_e32 v3, v1
	v_mov_b32_e32 v16, v1
	v_mov_b32_e32 v17, v1
	v_mov_b32_e32 v18, v1
	v_mov_b32_e32 v19, v1
	v_mov_b32_e32 v24, v1
	v_mov_b32_e32 v25, v1
	v_mov_b32_e32 v26, v1
	v_mov_b32_e32 v27, v1
	v_mov_b32_e32 v32, v1
	v_mov_b32_e32 v33, v1
	v_mov_b32_e32 v34, v1
	v_mov_b32_e32 v35, v1
	v_mov_b32_e32 v40, v1
	v_mov_b32_e32 v41, v1
	v_mov_b32_e32 v42, v1
	v_mov_b32_e32 v43, v1
	v_mov_b32_e32 v48, v1
	v_mov_b32_e32 v49, v1
	v_mov_b32_e32 v50, v1
	v_mov_b32_e32 v51, v1
	v_mov_b32_e32 v60, v1
	v_mov_b32_e32 v61, v1
	v_mov_b32_e32 v62, v1
	v_mov_b32_e32 v63, v1
	v_mov_b32_e32 v68, v1
	v_mov_b32_e32 v69, v1
	v_mov_b32_e32 v70, v1
	v_mov_b32_e32 v71, v1
	v_mov_b32_e32 v28, v1
	v_mov_b32_e32 v29, v1
	v_mov_b32_e32 v30, v1
	v_mov_b32_e32 v31, v1
	v_mov_b32_e32 v36, v1
	v_mov_b32_e32 v37, v1
	v_mov_b32_e32 v38, v1
	v_mov_b32_e32 v39, v1
	v_mov_b32_e32 v44, v1
	v_mov_b32_e32 v45, v1
	v_mov_b32_e32 v46, v1
	v_mov_b32_e32 v47, v1
	v_mov_b32_e32 v52, v1
	v_mov_b32_e32 v53, v1
	v_mov_b32_e32 v54, v1
	v_mov_b32_e32 v55, v1
	v_mov_b32_e32 v56, v1
	v_mov_b32_e32 v57, v1
	v_mov_b32_e32 v58, v1
	v_mov_b32_e32 v59, v1
	v_mov_b32_e32 v64, v1
	v_mov_b32_e32 v65, v1
	v_mov_b32_e32 v66, v1
	v_mov_b32_e32 v67, v1
	v_mov_b32_e32 v72, v1
	v_mov_b32_e32 v73, v1
	v_mov_b32_e32 v74, v1
	v_mov_b32_e32 v75, v1
	v_mov_b32_e32 v76, v1
	v_mov_b32_e32 v77, v1
	v_mov_b32_e32 v78, v1
	v_mov_b32_e32 v79, v1
	s_mov_b32 s15, s17
	s_lshl_b32 s17, s7, 7
	s_ashr_i32 s23, s17, 31
	s_add_u32 s20, s11, s17
	s_addc_u32 s21, s12, s23
	s_add_u32 s22, s4, s17
	s_addc_u32 s23, s5, s23
	s_add_i32 s17, s19, s14
.LBB1_7:
	v_add_u32_e32 v80, s15, v101
	ds_read_b128 v[92:95], v80 offset:16384
	ds_read_b128 v[96:99], v80 offset:17408
	ds_read_b128 v[108:111], v80 offset:18432
	ds_read_b128 v[112:115], v80 offset:19456
	ds_read_b128 v[116:119], v80 offset:32768
	ds_read_b128 v[120:123], v80 offset:33792
	ds_read_b128 v[124:127], v80 offset:34816
	s_add_i32 m0, s17, 0x4000
	ds_read_b128 v[128:131], v80 offset:35840
	global_load_lds_dwordx4 v84, s[20:21]
	v_add_u32_e32 v80, s15, v91
	ds_read_b128 v[132:135], v80
	ds_read_b128 v[136:139], v80 offset:1024
	s_add_i32 m0, s17, 0x6000
	ds_read_b128 v[140:143], v80 offset:2048
	global_load_lds_dwordx4 v88, s[20:21]
	ds_read_b128 v[144:147], v80 offset:3072
	ds_read_b128 v[148:151], v80 offset:4096
	s_mov_b32 m0, s17
	ds_read_b128 v[152:155], v80 offset:5120
	global_load_lds_dwordx4 v82, s[22:23]
	ds_read_b128 v[156:159], v80 offset:6144
	ds_read_b128 v[160:163], v80 offset:7168
	s_waitcnt vmcnt(3)
	s_waitcnt lgkmcnt(0)
	s_barrier
	s_setprio 1
	s_waitcnt lgkmcnt(0)
	v_mfma_f32_16x16x32_f16 v[76:79], v[92:95], v[132:135], v[76:79]
	s_add_u32 s20, s20, 0x40000
	s_addc_u32 s21, s21, 0
	s_add_i32 m0, s17, 0x8000
	v_mfma_f32_16x16x32_f16 v[72:75], v[108:111], v[132:135], v[72:75]
	global_load_lds_dwordx4 v84, s[20:21]
	s_add_i32 m0, s17, 0xa000
	v_mfma_f32_16x16x32_f16 v[64:67], v[92:95], v[140:143], v[64:67]
	global_load_lds_dwordx4 v88, s[20:21]
	s_add_i32 m0, s17, 0x2000
	v_mfma_f32_16x16x32_f16 v[56:59], v[108:111], v[140:143], v[56:59]
	global_load_lds_dwordx4 v86, s[22:23]
	v_mfma_f32_16x16x32_f16 v[76:79], v[96:99], v[136:139], v[76:79]
	s_add_i32 s7, s7, 1
	v_mfma_f32_16x16x32_f16 v[72:75], v[112:115], v[136:139], v[72:75]
	s_cmp_lg_u32 s7, 16
	v_mfma_f32_16x16x32_f16 v[64:67], v[96:99], v[144:147], v[64:67]
	s_cselect_b32 s7, s7, 0
	v_mfma_f32_16x16x32_f16 v[56:59], v[112:115], v[144:147], v[56:59]
	s_add_i32 s13, s13, -1
	v_mfma_f32_16x16x32_f16 v[52:55], v[92:95], v[148:151], v[52:55]
	s_mov_b32 s38, s15
	v_mfma_f32_16x16x32_f16 v[44:47], v[108:111], v[148:151], v[44:47]
	s_mov_b32 s15, s10
	v_mfma_f32_16x16x32_f16 v[36:39], v[92:95], v[156:159], v[36:39]
	s_mov_b32 s10, s14
	v_mfma_f32_16x16x32_f16 v[28:31], v[108:111], v[156:159], v[28:31]
	s_mov_b32 s14, s38
	v_mfma_f32_16x16x32_f16 v[52:55], v[96:99], v[152:155], v[52:55]
	s_lshl_b32 s17, s7, 7
	v_mfma_f32_16x16x32_f16 v[44:47], v[112:115], v[152:155], v[44:47]
	s_ashr_i32 s23, s17, 31
	v_mfma_f32_16x16x32_f16 v[36:39], v[96:99], v[160:163], v[36:39]
	s_add_u32 s20, s11, s17
	v_mfma_f32_16x16x32_f16 v[28:31], v[112:115], v[160:163], v[28:31]
	s_addc_u32 s21, s12, s23
	v_mfma_f32_16x16x32_f16 v[68:71], v[116:119], v[132:135], v[68:71]
	s_add_u32 s22, s4, s17
	v_mfma_f32_16x16x32_f16 v[60:63], v[124:127], v[132:135], v[60:63]
	s_addc_u32 s23, s5, s23
	v_mfma_f32_16x16x32_f16 v[48:51], v[116:119], v[140:143], v[48:51]
	s_add_i32 s17, s19, s14
	v_mfma_f32_16x16x32_f16 v[40:43], v[124:127], v[140:143], v[40:43]
	s_cmp_lg_u32 s13, 0
	v_mfma_f32_16x16x32_f16 v[68:71], v[120:123], v[136:139], v[68:71]
	v_mfma_f32_16x16x32_f16 v[60:63], v[128:131], v[136:139], v[60:63]
	v_mfma_f32_16x16x32_f16 v[48:51], v[120:123], v[144:147], v[48:51]
	v_mfma_f32_16x16x32_f16 v[40:43], v[128:131], v[144:147], v[40:43]
	v_mfma_f32_16x16x32_f16 v[32:35], v[116:119], v[148:151], v[32:35]
	v_mfma_f32_16x16x32_f16 v[24:27], v[124:127], v[148:151], v[24:27]
	v_mfma_f32_16x16x32_f16 v[16:19], v[116:119], v[156:159], v[16:19]
	v_mfma_f32_16x16x32_f16 v[0:3], v[124:127], v[156:159], v[0:3]
	v_mfma_f32_16x16x32_f16 v[32:35], v[120:123], v[152:155], v[32:35]
	v_mfma_f32_16x16x32_f16 v[24:27], v[128:131], v[152:155], v[24:27]
	v_mfma_f32_16x16x32_f16 v[16:19], v[120:123], v[160:163], v[16:19]
	v_mfma_f32_16x16x32_f16 v[0:3], v[128:131], v[160:163], v[0:3]
	s_setprio 0
	s_barrier
	s_cbranch_scc1 .LBB1_7
	s_mov_b32 s17, s15
	s_mov_b32 s15, s14
	s_sub_u32 s0, s0, s8
	s_subb_u32 s1, s1, s9
	s_add_u32 s0, s8, s0
	s_addc_u32 s1, s9, s1
	s_lshl_b32 s3, s3, 6
	s_or_b32 s3, s3, s16
	s_lshl_b32 s4, s6, 1
	v_lshrrev_b32_e32 v86, 5, v106
	v_pk_add_f32 v[78:79], v[22:23], v[78:79]
	v_pk_add_f32 v[76:77], v[20:21], v[76:77]
	v_pk_add_f32 v[72:73], v[12:13], v[72:73]
	s_or_b32 s3, s3, s4
	s_lshl_b32 s2, s2, 6
	v_cvt_pk_f16_f32 v76, v76, v77
	v_cvt_pk_f16_f32 v77, v78, v79
	v_cvt_pk_f16_f32 v78, v72, v73
	v_or_b32_e32 v72, s3, v86
	s_or_b32 s2, s2, s16
	v_ashrrev_i32_e32 v73, 31, v72
	v_pk_add_f32 v[70:71], v[10:11], v[70:71]
	v_pk_add_f32 v[68:69], v[8:9], v[68:69]
	v_pk_add_f32 v[60:61], v[4:5], v[60:61]
	s_or_b32 s2, s2, s4
	v_lshlrev_b64 v[72:73], 12, v[72:73]
	v_cvt_pk_f16_f32 v68, v68, v69
	v_cvt_pk_f16_f32 v69, v70, v71
	v_cvt_pk_f16_f32 v70, v60, v61
	v_or_b32_e32 v60, s2, v86
	v_mov_b32_e32 v91, 0
	v_pk_add_f32 v[74:75], v[14:15], v[74:75]
	v_lshl_add_u64 v[72:73], s[0:1], 0, v[72:73]
	v_ashrrev_i32_e32 v61, 31, v60
	v_cvt_pk_f16_f32 v79, v74, v75
	v_lshl_add_u64 v[74:75], v[72:73], 0, v[90:91]
	v_lshlrev_b64 v[60:61], 12, v[60:61]
	v_lshl_or_b32 v84, v102, 6, v100
	v_mov_b32_e32 v85, v91
	global_store_dwordx4 v[74:75], v[76:79], off sc1
	v_lshl_add_u64 v[74:75], s[0:1], 0, v[60:61]
	v_pk_add_f32 v[50:51], v[10:11], v[50:51]
	v_pk_add_f32 v[48:49], v[8:9], v[48:49]
	v_pk_add_f32 v[42:43], v[6:7], v[42:43]
	v_pk_add_f32 v[40:41], v[4:5], v[40:41]
	v_pk_add_f32 v[62:63], v[6:7], v[62:63]
	v_cvt_pk_f16_f32 v48, v48, v49
	v_cvt_pk_f16_f32 v49, v50, v51
	v_cvt_pk_f16_f32 v50, v40, v41
	v_cvt_pk_f16_f32 v51, v42, v43
	v_lshl_add_u64 v[40:41], v[74:75], 0, v[84:85]
	v_cvt_pk_f16_f32 v71, v62, v63
	v_lshl_add_u64 v[60:61], v[74:75], 0, v[90:91]
	global_store_dwordx4 v[40:41], v[48:51], off sc1
	v_pk_add_f32 v[42:43], v[22:23], v[54:55]
	v_pk_add_f32 v[40:41], v[20:21], v[52:53]
	v_lshl_or_b32 v80, v103, 6, v100
	v_lshl_or_b32 v82, v104, 6, v100
	v_mov_b32_e32 v81, v91
	v_mov_b32_e32 v83, v91
	global_store_dwordx4 v[60:61], v[68:71], off sc1
	v_pk_add_f32 v[62:63], v[22:23], v[66:67]
	v_pk_add_f32 v[60:61], v[20:21], v[64:65]
	v_pk_add_f32 v[58:59], v[14:15], v[58:59]
	v_pk_add_f32 v[56:57], v[12:13], v[56:57]
	v_cvt_pk_f16_f32 v40, v40, v41
	v_cvt_pk_f16_f32 v41, v42, v43
	v_pk_add_f32 v[46:47], v[14:15], v[46:47]
	v_pk_add_f32 v[42:43], v[12:13], v[44:45]
	v_pk_add_f32 v[34:35], v[10:11], v[34:35]
	v_pk_add_f32 v[32:33], v[8:9], v[32:33]
	v_pk_add_f32 v[26:27], v[6:7], v[26:27]
	v_pk_add_f32 v[24:25], v[4:5], v[24:25]
	v_pk_add_f32 v[22:23], v[22:23], v[38:39]
	v_pk_add_f32 v[20:21], v[20:21], v[36:37]
	v_pk_add_f32 v[14:15], v[14:15], v[30:31]
	v_pk_add_f32 v[12:13], v[12:13], v[28:29]
	v_pk_add_f32 v[10:11], v[10:11], v[18:19]
	v_pk_add_f32 v[8:9], v[8:9], v[16:17]
	v_pk_add_f32 v[2:3], v[6:7], v[2:3]
	v_pk_add_f32 v[0:1], v[4:5], v[0:1]
	v_cvt_pk_f16_f32 v60, v60, v61
	v_cvt_pk_f16_f32 v61, v62, v63
	v_cvt_pk_f16_f32 v62, v56, v57
	v_cvt_pk_f16_f32 v63, v58, v59
	v_lshl_add_u64 v[56:57], v[72:73], 0, v[84:85]
	v_cvt_pk_f16_f32 v42, v42, v43
	v_cvt_pk_f16_f32 v43, v46, v47
	v_lshl_add_u64 v[44:45], v[72:73], 0, v[80:81]
	v_cvt_pk_f16_f32 v32, v32, v33
	v_cvt_pk_f16_f32 v33, v34, v35
	v_cvt_pk_f16_f32 v34, v24, v25
	v_cvt_pk_f16_f32 v35, v26, v27
	v_lshl_add_u64 v[24:25], v[74:75], 0, v[80:81]
	v_cvt_pk_f16_f32 v20, v20, v21
	v_cvt_pk_f16_f32 v21, v22, v23
	v_cvt_pk_f16_f32 v22, v12, v13
	v_cvt_pk_f16_f32 v23, v14, v15
	v_lshl_add_u64 v[12:13], v[72:73], 0, v[82:83]
	v_cvt_pk_f16_f32 v8, v8, v9
	v_cvt_pk_f16_f32 v9, v10, v11
	v_cvt_pk_f16_f32 v10, v0, v1
	v_cvt_pk_f16_f32 v11, v2, v3
	v_lshl_add_u64 v[0:1], v[74:75], 0, v[82:83]
	global_store_dwordx4 v[56:57], v[60:63], off sc1
	global_store_dwordx4 v[44:45], v[40:43], off sc1
	global_store_dwordx4 v[24:25], v[32:35], off sc1
	global_store_dwordx4 v[12:13], v[20:23], off sc1
	global_store_dwordx4 v[0:1], v[8:11], off sc1
	s_waitcnt vmcnt(0)
	s_cmpk_gt_u32 s18, 0xff
	s_cbranch_scc1 .LBB1_10
	s_barrier

	.amdhsa_kernel _Z10kvq_kernelPKtS0_PtS1_S1_PKf
		.amdhsa_group_segment_fixed_size 0
		.amdhsa_private_segment_fixed_size 0
		.amdhsa_kernarg_size 48
		.amdhsa_user_sgpr_count 2
		.amdhsa_user_sgpr_dispatch_ptr 0
		.amdhsa_user_sgpr_queue_ptr 0
		.amdhsa_user_sgpr_kernarg_segment_ptr 1
		.amdhsa_user_sgpr_dispatch_id 0
		.amdhsa_user_sgpr_kernarg_preload_length 0
		.amdhsa_user_sgpr_kernarg_preload_offset 0
		.amdhsa_user_sgpr_private_segment_size 0
		.amdhsa_uses_dynamic_stack 0
		.amdhsa_enable_private_segment 0
		.amdhsa_system_sgpr_workgroup_id_x 1
		.amdhsa_system_sgpr_workgroup_id_y 0
		.amdhsa_system_sgpr_workgroup_id_z 0
		.amdhsa_system_sgpr_workgroup_info 0
		.amdhsa_system_vgpr_workitem_id 0
		.amdhsa_next_free_vgpr 172
		.amdhsa_next_free_sgpr 39
		.amdhsa_accum_offset 172
		.amdhsa_reserve_vcc 0
		.amdhsa_float_round_mode_32 0
		.amdhsa_float_round_mode_16_64 0
		.amdhsa_float_denorm_mode_32 3
		.amdhsa_float_denorm_mode_16_64 3
		.amdhsa_dx10_clamp 1
		.amdhsa_ieee_mode 1
		.amdhsa_fp16_overflow 0
		.amdhsa_tg_split 0
		.amdhsa_exception_fp_ieee_invalid_op 0
		.amdhsa_exception_fp_denorm_src 0
		.amdhsa_exception_fp_ieee_div_zero 0
		.amdhsa_exception_fp_ieee_overflow 0
		.amdhsa_exception_fp_ieee_underflow 0
		.amdhsa_exception_fp_ieee_inexact 0
		.amdhsa_exception_int_div_zero 0
	.end_amdhsa_kernel

.LBB2_2:
	v_and_b32_e32 v19, 15, v0
	v_lshlrev_b32_e32 v21, 6, v0
	s_movk_i32 s11, 0x3c0
	v_lshlrev_b32_e32 v0, 2, v0
	s_lshl_b32 s10, s16, 8
	v_lshlrev_b32_e32 v1, 2, v1
	v_lshl_or_b32 v86, s14, 6, v19
	v_lshl_or_b32 v19, v19, 6, v20
	v_and_or_b32 v20, v21, s11, v20
	v_and_b32_e32 v21, 32, v0
	s_lshl_b32 s11, s14, 13
	s_lshl_b32 s14, s1, 7
	s_barrier
	s_add_i32 s11, s11, 0
	s_add_i32 s14, s14, 0
	v_xad_u32 v0, v19, v21, s11
	v_xad_u32 v87, v20, v21, s14
	s_mov_b32 s14, 0x18000
	s_mov_b32 s11, 16
	v_mov_b32_e32 v19, v18
	v_mov_b32_e32 v20, v18
	v_mov_b32_e32 v21, v18
	v_mov_b32_e32 v70, v18
	v_mov_b32_e32 v71, v18
	v_mov_b32_e32 v72, v18
	v_mov_b32_e32 v73, v18
	v_mov_b32_e32 v58, v18
	v_mov_b32_e32 v59, v18
	v_mov_b32_e32 v60, v18
	v_mov_b32_e32 v61, v18
	v_mov_b32_e32 v54, v18
	v_mov_b32_e32 v55, v18
	v_mov_b32_e32 v56, v18
	v_mov_b32_e32 v57, v18
	v_mov_b32_e32 v42, v18
	v_mov_b32_e32 v43, v18
	v_mov_b32_e32 v44, v18
	v_mov_b32_e32 v45, v18
	v_mov_b32_e32 v38, v18
	v_mov_b32_e32 v39, v18
	v_mov_b32_e32 v40, v18
	v_mov_b32_e32 v41, v18
	v_mov_b32_e32 v26, v18
	v_mov_b32_e32 v27, v18
	v_mov_b32_e32 v28, v18
	v_mov_b32_e32 v29, v18
	v_mov_b32_e32 v22, v18
	v_mov_b32_e32 v23, v18
	v_mov_b32_e32 v24, v18
	v_mov_b32_e32 v25, v18
	v_mov_b32_e32 v78, v18
	v_mov_b32_e32 v79, v18
	v_mov_b32_e32 v80, v18
	v_mov_b32_e32 v81, v18
	v_mov_b32_e32 v74, v18
	v_mov_b32_e32 v75, v18
	v_mov_b32_e32 v76, v18
	v_mov_b32_e32 v77, v18
	v_mov_b32_e32 v66, v18
	v_mov_b32_e32 v67, v18
	v_mov_b32_e32 v68, v18
	v_mov_b32_e32 v69, v18
	v_mov_b32_e32 v62, v18
	v_mov_b32_e32 v63, v18
	v_mov_b32_e32 v64, v18
	v_mov_b32_e32 v65, v18
	v_mov_b32_e32 v50, v18
	v_mov_b32_e32 v51, v18
	v_mov_b32_e32 v52, v18
	v_mov_b32_e32 v53, v18
	v_mov_b32_e32 v46, v18
	v_mov_b32_e32 v47, v18
	v_mov_b32_e32 v48, v18
	v_mov_b32_e32 v49, v18
	v_mov_b32_e32 v34, v18
	v_mov_b32_e32 v35, v18
	v_mov_b32_e32 v36, v18
	v_mov_b32_e32 v37, v18
	v_mov_b32_e32 v30, v18
	v_mov_b32_e32 v31, v18
	v_mov_b32_e32 v32, v18
	v_mov_b32_e32 v33, v18
	s_mov_b32 s16, s15
	s_lshl_b32 s15, s7, 7
	s_ashr_i32 s17, s15, 31
	s_add_u32 s18, s4, s15
	s_addc_u32 s19, s5, s17
	s_add_u32 s20, s2, s15
	s_addc_u32 s21, s3, s17
	s_add_i32 s15, s6, s14
.LBB2_3:
	v_add_u32_e32 v116, s16, v87
	v_add_u32_e32 v148, s16, v0
	ds_read_b128 v[88:91], v116 offset:16384
	ds_read_b128 v[92:95], v116 offset:17408
	ds_read_b128 v[96:99], v116 offset:18432
	ds_read_b128 v[100:103], v116 offset:19456
	ds_read_b128 v[104:107], v116 offset:32768
	ds_read_b128 v[108:111], v116 offset:33792
	ds_read_b128 v[112:115], v116 offset:34816
	s_add_i32 m0, s15, 0x4000
	ds_read_b128 v[116:119], v116 offset:35840
	global_load_lds_dwordx4 v82, s[18:19]
	ds_read_b128 v[120:123], v148
	ds_read_b128 v[124:127], v148 offset:1024
	s_add_i32 m0, s15, 0x6000
	ds_read_b128 v[128:131], v148 offset:2048
	global_load_lds_dwordx4 v84, s[18:19]
	ds_read_b128 v[132:135], v148 offset:3072
	ds_read_b128 v[136:139], v148 offset:4096
	s_mov_b32 m0, s15
	ds_read_b128 v[140:143], v148 offset:5120
	global_load_lds_dwordx4 v82, s[20:21]
	ds_read_b128 v[144:147], v148 offset:6144
	ds_read_b128 v[148:151], v148 offset:7168
	s_waitcnt vmcnt(3)
	s_waitcnt lgkmcnt(0)
	s_barrier
	s_setprio 1
	s_waitcnt lgkmcnt(0)
	v_mfma_f32_16x16x32_f16 v[18:21], v[88:91], v[120:123], v[18:21]
	s_add_u32 s18, s18, 0x40000
	s_addc_u32 s19, s19, 0
	s_add_i32 m0, s15, 0x8000
	v_mfma_f32_16x16x32_f16 v[70:73], v[96:99], v[120:123], v[70:73]
	global_load_lds_dwordx4 v82, s[18:19]
	s_add_i32 m0, s15, 0xa000
	v_mfma_f32_16x16x32_f16 v[58:61], v[88:91], v[128:131], v[58:61]
	global_load_lds_dwordx4 v84, s[18:19]
	s_add_i32 m0, s15, 0x2000
	v_mfma_f32_16x16x32_f16 v[54:57], v[96:99], v[128:131], v[54:57]
	global_load_lds_dwordx4 v84, s[20:21]
	v_mfma_f32_16x16x32_f16 v[18:21], v[92:95], v[124:127], v[18:21]
	s_add_i32 s7, s7, 1
	v_mfma_f32_16x16x32_f16 v[70:73], v[100:103], v[124:127], v[70:73]
	s_cmp_lg_u32 s7, 16
	v_mfma_f32_16x16x32_f16 v[58:61], v[92:95], v[132:135], v[58:61]
	s_cselect_b32 s7, s7, 0
	v_mfma_f32_16x16x32_f16 v[54:57], v[100:103], v[132:135], v[54:57]
	s_add_i32 s11, s11, -1
	v_mfma_f32_16x16x32_f16 v[42:45], v[88:91], v[136:139], v[42:45]
	s_mov_b32 s22, s16
	v_mfma_f32_16x16x32_f16 v[38:41], v[96:99], v[136:139], v[38:41]
	s_mov_b32 s16, s13
	v_mfma_f32_16x16x32_f16 v[26:29], v[88:91], v[144:147], v[26:29]
	s_mov_b32 s13, s14
	v_mfma_f32_16x16x32_f16 v[22:25], v[96:99], v[144:147], v[22:25]
	s_mov_b32 s14, s22
	v_mfma_f32_16x16x32_f16 v[42:45], v[92:95], v[140:143], v[42:45]
	s_lshl_b32 s15, s7, 7
	v_mfma_f32_16x16x32_f16 v[38:41], v[100:103], v[140:143], v[38:41]
	s_ashr_i32 s17, s15, 31
	v_mfma_f32_16x16x32_f16 v[26:29], v[92:95], v[148:151], v[26:29]
	s_add_u32 s18, s4, s15
	v_mfma_f32_16x16x32_f16 v[22:25], v[100:103], v[148:151], v[22:25]
	s_addc_u32 s19, s5, s17
	v_mfma_f32_16x16x32_f16 v[78:81], v[104:107], v[120:123], v[78:81]
	s_add_u32 s20, s2, s15
	v_mfma_f32_16x16x32_f16 v[74:77], v[112:115], v[120:123], v[74:77]
	s_addc_u32 s21, s3, s17
	v_mfma_f32_16x16x32_f16 v[66:69], v[104:107], v[128:131], v[66:69]
	s_add_i32 s15, s6, s14
	v_mfma_f32_16x16x32_f16 v[62:65], v[112:115], v[128:131], v[62:65]
	s_cmp_lg_u32 s11, 0
	v_mfma_f32_16x16x32_f16 v[78:81], v[108:111], v[124:127], v[78:81]
	v_mfma_f32_16x16x32_f16 v[74:77], v[116:119], v[124:127], v[74:77]
	v_mfma_f32_16x16x32_f16 v[66:69], v[108:111], v[132:135], v[66:69]
	v_mfma_f32_16x16x32_f16 v[62:65], v[116:119], v[132:135], v[62:65]
	v_mfma_f32_16x16x32_f16 v[50:53], v[104:107], v[136:139], v[50:53]
	v_mfma_f32_16x16x32_f16 v[46:49], v[112:115], v[136:139], v[46:49]
	v_mfma_f32_16x16x32_f16 v[34:37], v[104:107], v[144:147], v[34:37]
	v_mfma_f32_16x16x32_f16 v[30:33], v[112:115], v[144:147], v[30:33]
	v_mfma_f32_16x16x32_f16 v[50:53], v[108:111], v[140:143], v[50:53]
	v_mfma_f32_16x16x32_f16 v[46:49], v[116:119], v[140:143], v[46:49]
	v_mfma_f32_16x16x32_f16 v[34:37], v[108:111], v[148:151], v[34:37]
	v_mfma_f32_16x16x32_f16 v[30:33], v[116:119], v[148:151], v[30:33]
	s_setprio 0
	s_barrier
	s_cbranch_scc1 .LBB2_3
	s_mov_b32 s15, s16
	s_mov_b32 s16, s14
	v_lshl_add_u32 v0, s0, 7, v86
	v_or_b32_e32 v88, s10, v1
	v_ashrrev_i32_e32 v1, 31, v0
	v_lshlrev_b64 v[82:83], 12, v[0:1]
	v_or_b32_e32 v88, s1, v88
	v_lshl_add_u64 v[82:83], s[8:9], 0, v[82:83]
	v_lshlrev_b32_e32 v88, 2, v88
	v_mov_b32_e32 v89, 0
	v_or_b32_e32 v84, 16, v0
	v_lshl_add_u64 v[82:83], v[82:83], 0, v[88:89]
	v_pk_add_f32 v[20:21], v[16:17], v[20:21]
	v_pk_add_f32 v[18:19], v[14:15], v[18:19]
	v_ashrrev_i32_e32 v85, 31, v84
	global_store_dwordx4 v[82:83], v[18:21], off sc1
	v_lshlrev_b64 v[84:85], 12, v[84:85]
	v_lshl_add_u64 v[84:85], s[8:9], 0, v[84:85]
	v_pk_add_f32 v[20:21], v[12:13], v[72:73]
	v_pk_add_f32 v[18:19], v[10:11], v[70:71]
	global_store_dwordx4 v[82:83], v[18:21], off offset:64 sc1
	v_or_b32_e32 v86, 32, v0
	v_lshl_add_u64 v[84:85], v[84:85], 0, v[88:89]
	v_pk_add_f32 v[20:21], v[8:9], v[80:81]
	v_pk_add_f32 v[18:19], v[6:7], v[78:79]
	global_store_dwordx4 v[82:83], v[18:21], off offset:512 sc1
	v_ashrrev_i32_e32 v87, 31, v86
	v_lshlrev_b64 v[86:87], 12, v[86:87]
	v_pk_add_f32 v[20:21], v[4:5], v[76:77]
	v_pk_add_f32 v[18:19], v[2:3], v[74:75]
	global_store_dwordx4 v[82:83], v[18:21], off offset:576 sc1
	v_lshl_add_u64 v[86:87], s[8:9], 0, v[86:87]
	v_or_b32_e32 v0, 48, v0
	v_pk_add_f32 v[20:21], v[16:17], v[60:61]
	v_pk_add_f32 v[18:19], v[14:15], v[58:59]
	global_store_dwordx4 v[84:85], v[18:21], off sc1
	v_ashrrev_i32_e32 v1, 31, v0
	v_lshl_add_u64 v[86:87], v[86:87], 0, v[88:89]
	v_pk_add_f32 v[20:21], v[12:13], v[56:57]
	v_pk_add_f32 v[18:19], v[10:11], v[54:55]
	global_store_dwordx4 v[84:85], v[18:21], off offset:64 sc1
	v_lshlrev_b64 v[0:1], 12, v[0:1]
	v_lshl_add_u64 v[0:1], s[8:9], 0, v[0:1]
	v_pk_add_f32 v[20:21], v[8:9], v[68:69]
	v_pk_add_f32 v[18:19], v[6:7], v[66:67]
	global_store_dwordx4 v[84:85], v[18:21], off offset:512 sc1
	v_lshl_add_u64 v[0:1], v[0:1], 0, v[88:89]
	s_cmpk_gt_u32 s12, 0xff
	v_pk_add_f32 v[20:21], v[4:5], v[64:65]
	v_pk_add_f32 v[18:19], v[2:3], v[62:63]
	global_store_dwordx4 v[84:85], v[18:21], off offset:576 sc1
	s_nop 1
	v_pk_add_f32 v[20:21], v[16:17], v[44:45]
	v_pk_add_f32 v[18:19], v[14:15], v[42:43]
	global_store_dwordx4 v[86:87], v[18:21], off sc1
	v_pk_add_f32 v[16:17], v[16:17], v[28:29]
	v_pk_add_f32 v[14:15], v[14:15], v[26:27]
	v_pk_add_f32 v[20:21], v[12:13], v[40:41]
	v_pk_add_f32 v[18:19], v[10:11], v[38:39]
	global_store_dwordx4 v[86:87], v[18:21], off offset:64 sc1
	v_pk_add_f32 v[12:13], v[12:13], v[24:25]
	v_pk_add_f32 v[10:11], v[10:11], v[22:23]
	v_pk_add_f32 v[20:21], v[8:9], v[52:53]
	v_pk_add_f32 v[18:19], v[6:7], v[50:51]
	global_store_dwordx4 v[86:87], v[18:21], off offset:512 sc1
	v_pk_add_f32 v[8:9], v[8:9], v[36:37]
	v_pk_add_f32 v[6:7], v[6:7], v[34:35]
	v_pk_add_f32 v[20:21], v[4:5], v[48:49]
	v_pk_add_f32 v[18:19], v[2:3], v[46:47]
	v_pk_add_f32 v[4:5], v[4:5], v[32:33]
	v_pk_add_f32 v[2:3], v[2:3], v[30:31]
	global_store_dwordx4 v[86:87], v[18:21], off offset:576 sc1
	global_store_dwordx4 v[0:1], v[14:17], off sc1
	global_store_dwordx4 v[0:1], v[10:13], off offset:64 sc1
	global_store_dwordx4 v[0:1], v[6:9], off offset:512 sc1
	global_store_dwordx4 v[0:1], v[2:5], off offset:576 sc1
	s_waitcnt vmcnt(0)
	s_cbranch_scc1 .LBB2_6
	s_barrier

	.amdhsa_kernel _Z11out2_kernelPKtS0_PfPKf
		.amdhsa_group_segment_fixed_size 0
		.amdhsa_private_segment_fixed_size 0
		.amdhsa_kernarg_size 32
		.amdhsa_user_sgpr_count 2
		.amdhsa_user_sgpr_dispatch_ptr 0
		.amdhsa_user_sgpr_queue_ptr 0
		.amdhsa_user_sgpr_kernarg_segment_ptr 1
		.amdhsa_user_sgpr_dispatch_id 0
		.amdhsa_user_sgpr_kernarg_preload_length 0
		.amdhsa_user_sgpr_kernarg_preload_offset 0
		.amdhsa_user_sgpr_private_segment_size 0
		.amdhsa_uses_dynamic_stack 0
		.amdhsa_enable_private_segment 0
		.amdhsa_system_sgpr_workgroup_id_x 1
		.amdhsa_system_sgpr_workgroup_id_y 0
		.amdhsa_system_sgpr_workgroup_id_z 0
		.amdhsa_system_sgpr_workgroup_info 0
		.amdhsa_system_vgpr_workitem_id 0
		.amdhsa_next_free_vgpr 154
		.amdhsa_next_free_sgpr 23
		.amdhsa_accum_offset 156
		.amdhsa_reserve_vcc 0
		.amdhsa_float_round_mode_32 0
		.amdhsa_float_round_mode_16_64 0
		.amdhsa_float_denorm_mode_32 3
		.amdhsa_float_denorm_mode_16_64 3
		.amdhsa_dx10_clamp 1
		.amdhsa_ieee_mode 1
		.amdhsa_fp16_overflow 0
		.amdhsa_tg_split 0
		.amdhsa_exception_fp_ieee_invalid_op 0
		.amdhsa_exception_fp_denorm_src 0
		.amdhsa_exception_fp_ieee_div_zero 0
		.amdhsa_exception_fp_ieee_overflow 0
		.amdhsa_exception_fp_ieee_underflow 0
		.amdhsa_exception_fp_ieee_inexact 0
		.amdhsa_exception_int_div_zero 0
	.end_amdhsa_kernel

amdhsa.kernels:
  - .agpr_count:     0
    .args:
      - .actual_access:  read_only
        .address_space:  global
        .offset:         0
        .size:           8
        .value_kind:     global_buffer
      - .actual_access:  read_only
        .address_space:  global
        .offset:         8
        .size:           8
        .value_kind:     global_buffer
      - .actual_access:  read_only
        .address_space:  global
        .offset:         16
        .size:           8
        .value_kind:     global_buffer
      - .actual_access:  write_only
        .address_space:  global
        .offset:         24
        .size:           8
        .value_kind:     global_buffer
      - .actual_access:  write_only
        .address_space:  global
        .offset:         32
        .size:           8
        .value_kind:     global_buffer
      - .actual_access:  write_only
        .address_space:  global
        .offset:         40
        .size:           8
        .value_kind:     global_buffer
    .group_segment_fixed_size: 0
    .kernarg_segment_align: 8
    .kernarg_segment_size: 48
    .language:       OpenCL C
    .language_version:
      - 2
      - 0
    .max_flat_workgroup_size: 256
    .name:           _Z10cvt_kernelPKfS0_S0_PtS1_S1_
    .private_segment_fixed_size: 0
    .sgpr_count:     16
    .sgpr_spill_count: 0
    .symbol:         _Z10cvt_kernelPKfS0_S0_PtS1_S1_.kd
    .uniform_work_group_size: 1
    .uses_dynamic_stack: false
    .vgpr_count:     40
    .vgpr_spill_count: 0
    .wavefront_size: 64
  - .agpr_count:     0
    .args:
      - .address_space:  global
        .offset:         0
        .size:           8
        .value_kind:     global_buffer
      - .address_space:  global
        .offset:         8
        .size:           8
        .value_kind:     global_buffer
      - .address_space:  global
        .offset:         16
        .size:           8
        .value_kind:     global_buffer
      - .address_space:  global
        .offset:         24
        .size:           8
        .value_kind:     global_buffer
      - .address_space:  global
        .offset:         32
        .size:           8
        .value_kind:     global_buffer
      - .address_space:  global
        .offset:         40
        .size:           8
        .value_kind:     global_buffer
    .group_segment_fixed_size: 0
    .kernarg_segment_align: 8
    .kernarg_segment_size: 48
    .language:       OpenCL C
    .language_version:
      - 2
      - 0
    .max_flat_workgroup_size: 512
    .name:           _Z10kvq_kernelPKtS0_PtS1_S1_PKf
    .private_segment_fixed_size: 0
    .sgpr_count:     45
    .sgpr_spill_count: 0
    .symbol:         _Z10kvq_kernelPKtS0_PtS1_S1_PKf.kd
    .uniform_work_group_size: 1
    .uses_dynamic_stack: false
    .vgpr_count:     172
    .vgpr_spill_count: 0
    .wavefront_size: 64
  - .agpr_count:     0
    .args:
      - .address_space:  global
        .offset:         0
        .size:           8
        .value_kind:     global_buffer
      - .address_space:  global
        .offset:         8
        .size:           8
        .value_kind:     global_buffer
      - .address_space:  global
        .offset:         16
        .size:           8
        .value_kind:     global_buffer
      - .address_space:  global
        .offset:         24
        .size:           8
        .value_kind:     global_buffer
    .group_segment_fixed_size: 0
    .kernarg_segment_align: 8
    .kernarg_segment_size: 32
    .language:       OpenCL C
    .language_version:
      - 2
      - 0
    .max_flat_workgroup_size: 512
    .name:           _Z11out2_kernelPKtS0_PfPKf
    .private_segment_fixed_size: 0
    .sgpr_count:     29
    .sgpr_spill_count: 0
    .symbol:         _Z11out2_kernelPKtS0_PfPKf.kd
    .uniform_work_group_size: 1
    .uses_dynamic_stack: false
    .vgpr_count:     154
    .vgpr_spill_count: 0
    .wavefront_size: 64
  - .agpr_count:     0
    .args:
      - .address_space:  global
        .offset:         0
        .size:           8
        .value_kind:     global_buffer
      - .address_space:  global
        .offset:         8
        .size:           8
        .value_kind:     global_buffer
      - .address_space:  global
        .offset:         16
        .size:           8
        .value_kind:     global_buffer
      - .address_space:  global
        .offset:         24
        .size:           8
        .value_kind:     global_buffer
      - .offset:         32
        .size:           4
        .value_kind:     hidden_block_count_x
      - .offset:         36
        .size:           4
        .value_kind:     hidden_block_count_y
      - .offset:         40
        .size:           4
        .value_kind:     hidden_block_count_z
      - .offset:         44
        .size:           2
        .value_kind:     hidden_group_size_x
      - .offset:         46
        .size:           2
        .value_kind:     hidden_group_size_y
      - .offset:         48
        .size:           2
        .value_kind:     hidden_group_size_z
      - .offset:         50
        .size:           2
        .value_kind:     hidden_remainder_x
      - .offset:         52
        .size:           2
        .value_kind:     hidden_remainder_y
      - .offset:         54
        .size:           2
        .value_kind:     hidden_remainder_z
      - .offset:         72
        .size:           8
        .value_kind:     hidden_global_offset_x
      - .offset:         80
        .size:           8
        .value_kind:     hidden_global_offset_y
      - .offset:         88
        .size:           8
        .value_kind:     hidden_global_offset_z
      - .offset:         96
        .size:           2
        .value_kind:     hidden_grid_dims
      - .offset:         152
        .size:           4
        .value_kind:     hidden_dynamic_lds_size
    .group_segment_fixed_size: 0
    .kernarg_segment_align: 8
    .kernarg_segment_size: 288
    .language:       OpenCL C
    .language_version:
      - 2
      - 0
    .max_flat_workgroup_size: 512
    .name:           _Z11attn_kernelPKtS0_S0_Pt
    .private_segment_fixed_size: 0
    .sgpr_count:     56
    .sgpr_spill_count: 0
    .symbol:         _Z11attn_kernelPKtS0_S0_Pt.kd
    .uniform_work_group_size: 1
    .uses_dynamic_stack: false
    .vgpr_count:     256
    .vgpr_spill_count: 0
    .wavefront_size: 64
